# speedup vs baseline: 1.0057x; 1.0057x over previous
_Z10fin_kernelPKfS0_Pf:
	s_load_dwordx4 s[4:7], s[0:1], 0x0
	s_load_dwordx2 s[8:9], s[0:1], 0x10
	s_lshl_b32 s3, s2, 1
	s_mul_i32 s0, s2, 0x8b20
	s_mul_hi_i32 s1, s3, 0x4590
	s_lshl_b32 s10, s2, 14
	v_mov_b32_e32 v50, 0
	s_waitcnt lgkmcnt(0)
	s_add_u32 s10, s8, s10
	s_addc_u32 s11, s9, 0
	s_add_u32 s0, s4, s0
	s_addc_u32 s1, s5, s1
	v_lshlrev_b32_e32 v1, 5, v0
	global_load_dwordx4 v[2:5], v1, s[0:1]
	global_load_dwordx4 v[6:9], v1, s[0:1] offset:16
	s_or_b32 s0, s3, 1
	s_mul_hi_i32 s1, s0, 0x4590
	s_mulk_i32 s0, 0x4590
	s_add_u32 s0, s4, s0
	s_addc_u32 s1, s5, s1
	global_load_dwordx4 v[10:13], v1, s[0:1]
	global_load_dwordx4 v[14:17], v1, s[0:1] offset:16
	v_lshlrev_b32_e32 v1, 1, v0
	v_mov_b32_e32 v35, 0
	v_lshrrev_b32_e32 v18, 1, v0
	v_and_b32_e32 v34, 0x180, v1
	v_mov_b32_e32 v37, v35
	v_and_b32_e32 v36, 16, v18
	v_lshl_add_u64 v[18:19], s[6:7], 0, v[34:35]
	v_lshl_add_u64 v[38:39], v[18:19], 0, v[36:37]
	global_load_dwordx4 v[18:21], v[38:39], off
	global_load_dwordx4 v[22:25], v[38:39], off offset:32
	global_load_dwordx4 v[26:29], v[38:39], off offset:64
	global_load_dwordx4 v[30:33], v[38:39], off offset:96
	global_load_dword v50, v50, s[10:11]
	v_and_b32_e32 v0, 31, v0
	v_lshl_or_b32 v0, s2, 5, v0
	v_ashrrev_i32_e32 v1, 31, v0
	v_lshlrev_b64 v[0:1], 9, v[0:1]
	v_lshl_add_u64 v[0:1], s[8:9], 0, v[0:1]
	v_lshl_add_u64 v[0:1], v[0:1], 0, v[34:35]
	v_lshl_add_u64 v[34:35], v[0:1], 0, v[36:37]
	s_waitcnt vmcnt(8)
	v_cvt_f32_f16_e32 v0, v2
	v_cvt_f32_f16_sdwa v1, v2 dst_sel:DWORD dst_unused:UNUSED_PAD src0_sel:WORD_1
	v_cvt_f32_f16_e32 v2, v3
	v_cvt_f32_f16_sdwa v3, v3 dst_sel:DWORD dst_unused:UNUSED_PAD src0_sel:WORD_1
	v_cvt_f32_f16_e32 v36, v4
	v_cvt_f32_f16_sdwa v37, v4 dst_sel:DWORD dst_unused:UNUSED_PAD src0_sel:WORD_1
	s_waitcnt vmcnt(6)
	v_cvt_f32_f16_e32 v42, v10
	v_cvt_f32_f16_sdwa v43, v10 dst_sel:DWORD dst_unused:UNUSED_PAD src0_sel:WORD_1
	v_cvt_f32_f16_e32 v10, v11
	v_cvt_f32_f16_sdwa v11, v11 dst_sel:DWORD dst_unused:UNUSED_PAD src0_sel:WORD_1
	v_cvt_f32_f16_e32 v4, v5
	v_cvt_f32_f16_sdwa v5, v5 dst_sel:DWORD dst_unused:UNUSED_PAD src0_sel:WORD_1
	v_cvt_f32_f16_e32 v38, v6
	v_cvt_f32_f16_sdwa v39, v6 dst_sel:DWORD dst_unused:UNUSED_PAD src0_sel:WORD_1
	v_cvt_f32_f16_e32 v6, v7
	v_cvt_f32_f16_sdwa v7, v7 dst_sel:DWORD dst_unused:UNUSED_PAD src0_sel:WORD_1
	v_cvt_f32_f16_e32 v40, v8
	v_cvt_f32_f16_sdwa v41, v8 dst_sel:DWORD dst_unused:UNUSED_PAD src0_sel:WORD_1
	v_cvt_f32_f16_e32 v8, v9
	v_cvt_f32_f16_sdwa v9, v9 dst_sel:DWORD dst_unused:UNUSED_PAD src0_sel:WORD_1
	v_cvt_f32_f16_e32 v44, v12
	v_cvt_f32_f16_sdwa v45, v12 dst_sel:DWORD dst_unused:UNUSED_PAD src0_sel:WORD_1
	v_cvt_f32_f16_e32 v12, v13
	v_cvt_f32_f16_sdwa v13, v13 dst_sel:DWORD dst_unused:UNUSED_PAD src0_sel:WORD_1
	s_waitcnt vmcnt(5)
	v_cvt_f32_f16_e32 v46, v14
	v_cvt_f32_f16_sdwa v47, v14 dst_sel:DWORD dst_unused:UNUSED_PAD src0_sel:WORD_1
	v_cvt_f32_f16_e32 v14, v15
	v_cvt_f32_f16_sdwa v15, v15 dst_sel:DWORD dst_unused:UNUSED_PAD src0_sel:WORD_1
	v_cvt_f32_f16_e32 v48, v16
	v_cvt_f32_f16_sdwa v49, v16 dst_sel:DWORD dst_unused:UNUSED_PAD src0_sel:WORD_1
	v_cvt_f32_f16_e32 v16, v17
	v_cvt_f32_f16_sdwa v17, v17 dst_sel:DWORD dst_unused:UNUSED_PAD src0_sel:WORD_1
	v_pk_add_f32 v[0:1], v[0:1], v[42:43]
	v_pk_add_f32 v[2:3], v[2:3], v[10:11]
	v_pk_add_f32 v[10:11], v[36:37], v[44:45]
	v_pk_add_f32 v[12:13], v[4:5], v[12:13]
	v_pk_add_f32 v[36:37], v[38:39], v[46:47]
	v_pk_add_f32 v[14:15], v[6:7], v[14:15]
	v_pk_add_f32 v[38:39], v[40:41], v[48:49]
	v_pk_add_f32 v[16:17], v[8:9], v[16:17]
	s_waitcnt vmcnt(4)
	v_pk_add_f32 v[0:1], v[0:1], v[18:19]
	v_pk_add_f32 v[2:3], v[2:3], v[20:21]
	s_waitcnt vmcnt(3)
	v_pk_add_f32 v[4:5], v[10:11], v[22:23]
	v_pk_add_f32 v[6:7], v[12:13], v[24:25]
	s_waitcnt vmcnt(2)
	v_pk_add_f32 v[8:9], v[36:37], v[26:27]
	v_pk_add_f32 v[10:11], v[14:15], v[28:29]
	s_waitcnt vmcnt(1)
	v_pk_add_f32 v[12:13], v[38:39], v[30:31]
	v_pk_add_f32 v[14:15], v[16:17], v[32:33]
	global_store_dwordx4 v[34:35], v[0:3], off
	global_store_dwordx4 v[34:35], v[4:7], off offset:32
	global_store_dwordx4 v[34:35], v[8:11], off offset:64
	global_store_dwordx4 v[34:35], v[12:15], off offset:96
	s_waitcnt vmcnt(4)
	s_endpgm
